# speedup vs baseline: 1.1082x; 1.0143x over previous
.LBB2_15:
	s_or_b64 exec, exec, s[6:7]
	s_waitcnt vmcnt(5)
	v_fma_mix_f32 v112, v6, 1.0, v112 op_sel_hi:[1,0,0]
	v_fma_mix_f32 v111, v6, 1.0, v111 op_sel:[1,0,0] op_sel_hi:[1,0,0]
	v_fma_mix_f32 v110, v7, 1.0, v110 op_sel_hi:[1,0,0]
	v_fma_mix_f32 v108, v7, 1.0, v108 op_sel:[1,0,0] op_sel_hi:[1,0,0]
	v_fma_mix_f32 v106, v8, 1.0, v106 op_sel_hi:[1,0,0]
	v_fma_mix_f32 v105, v8, 1.0, v105 op_sel:[1,0,0] op_sel_hi:[1,0,0]
	v_fma_mix_f32 v103, v9, 1.0, v103 op_sel_hi:[1,0,0]
	v_fma_mix_f32 v75, v9, 1.0, v75 op_sel:[1,0,0] op_sel_hi:[1,0,0]
	v_sub_u32_e32 v6, v102, v89
	v_add_u32_e32 v6, -12, v6
	v_cmp_lt_u32_e64 s[0:1], v6, v5
	s_cmp_eq_u64 s[0:1], 0
	s_cbranch_scc1 .Lmid_exit_l1
	s_setprio 3
	ds_bpermute_b32 v6, v91, v104
	ds_bpermute_b32 v7, v92, v104
	ds_bpermute_b32 v10, v93, v104
	ds_bpermute_b32 v11, v94, v104
	s_waitcnt lgkmcnt(3)
	v_lshlrev_b32_e32 v6, 7, v6
	s_waitcnt lgkmcnt(2)
	v_lshlrev_b32_e32 v8, 7, v7
	v_and_b32_e32 v76, 0x7fff80, v6
	v_lshl_add_u64 v[6:7], v[78:79], 0, v[76:77]
	v_and_b32_e32 v76, 0x7fff80, v8
	v_lshl_add_u64 v[8:9], v[78:79], 0, v[76:77]
	global_load_dwordx4 v[26:29], v[6:7], off
	global_load_dwordx4 v[18:21], v[8:9], off
	s_waitcnt lgkmcnt(1)
	v_lshlrev_b32_e32 v6, 7, v10
	v_and_b32_e32 v76, 0x7fff80, v6
	s_waitcnt lgkmcnt(0)
	v_lshlrev_b32_e32 v8, 7, v11
	v_lshl_add_u64 v[6:7], v[78:79], 0, v[76:77]
	v_and_b32_e32 v76, 0x7fff80, v8
	v_lshl_add_u64 v[8:9], v[78:79], 0, v[76:77]
	global_load_dwordx4 v[10:13], v[6:7], off
	s_nop 0
	global_load_dwordx4 v[6:9], v[8:9], off
	s_setprio 1
	v_and_b32_e32 v76, 16, v80
	v_cmp_ne_u32_e64 s[0:1], 0, v76
	s_and_saveexec_b64 s[6:7], s[0:1]
	s_cbranch_execz .LBB2_17
	v_and_b32_e32 v76, 63, v109
	v_mul_u32_u24_e32 v76, 0x120, v76
	v_or_b32_e32 v76, v84, v76
	ds_read2_b32 v[114:115], v76 offset1:8
	ds_read2_b32 v[116:117], v76 offset0:16 offset1:24
	ds_read2_b32 v[118:119], v76 offset0:32 offset1:40
	s_waitcnt lgkmcnt(2)
	v_add_f32_e32 v81, v112, v114
	v_add_f32_e32 v109, v111, v115
	s_waitcnt lgkmcnt(1)
	v_add_f32_e32 v110, v110, v116
	ds_write2_b32 v76, v81, v109 offset1:8
	v_add_f32_e32 v81, v108, v117
	ds_read2_b32 v[108:109], v76 offset0:48 offset1:56
	ds_write2_b32 v76, v110, v81 offset0:16 offset1:24
	s_waitcnt lgkmcnt(3)
	v_add_f32_e32 v81, v106, v118
	ds_bpermute_b32 v106, v97, v101
	v_add_f32_e32 v105, v105, v119
	ds_write2_b32 v76, v81, v105 offset0:32 offset1:40
	s_waitcnt lgkmcnt(3)
	v_add_f32_e32 v81, v103, v108
	v_add_f32_e32 v75, v75, v109
	ds_write2_b32 v76, v81, v75 offset0:48 offset1:56
	s_waitcnt lgkmcnt(2)
	v_lshrrev_b32_e32 v109, 16, v106
	v_mov_b32_e32 v75, 0
	v_mov_b32_e32 v112, 0
	v_mov_b32_e32 v111, 0
	v_mov_b32_e32 v110, 0
	v_mov_b32_e32 v108, 0
	v_mov_b32_e32 v106, 0
	v_mov_b32_e32 v105, 0
	v_mov_b32_e32 v103, 0

.Lmid_exit_l1:
	s_waitcnt vmcnt(0) lgkmcnt(0)
	s_branch .LBB2_23

.LBB3_15:
	s_or_b64 exec, exec, s[4:5]
	v_cvt_f32_ubyte1_e32 v13, v6
	v_cvt_f32_ubyte0_e32 v12, v6
	v_fmac_f32_e32 v78, v12, v46
	v_fmac_f32_e32 v79, v13, v46
	v_cvt_f32_ubyte3_e32 v13, v6
	v_cvt_f32_ubyte2_e32 v12, v6
	v_fmac_f32_e32 v76, v12, v46
	v_fmac_f32_e32 v77, v13, v46
	v_cvt_f32_ubyte1_e32 v13, v7
	v_cvt_f32_ubyte0_e32 v12, v7
	v_fma_f32 v74, v12, v46, v68
	v_fma_f32 v75, v13, v46, v69
	v_cvt_f32_ubyte3_e32 v13, v7
	v_cvt_f32_ubyte2_e32 v12, v7
	v_cvt_f32_ubyte1_e32 v7, v8
	v_cvt_f32_ubyte0_e32 v6, v8
	v_fma_f32 v70, v6, v46, v56
	v_fma_f32 v71, v7, v46, v57
	v_cvt_f32_ubyte3_e32 v7, v8
	v_cvt_f32_ubyte2_e32 v6, v8
	v_fma_f32 v68, v6, v46, v30
	v_fma_f32 v69, v7, v46, v31
	v_cvt_f32_ubyte1_e32 v7, v9
	v_cvt_f32_ubyte0_e32 v6, v9
	v_fma_f32 v72, v12, v46, v66
	v_fma_f32 v73, v13, v46, v67
	v_fma_f32 v66, v6, v46, v20
	v_fma_f32 v67, v7, v46, v21
	v_cvt_f32_ubyte3_e32 v7, v9
	v_cvt_f32_ubyte2_e32 v6, v9
	v_fma_f32 v64, v6, v46, v10
	v_fma_f32 v65, v7, v46, v11
	v_sub_u32_e32 v12, v94, v47
	v_add_u32_e32 v12, -12, v12
	v_cmp_lt_u32_e64 s[0:1], v12, v5
	s_cmp_eq_u64 s[0:1], 0
	s_cbranch_scc1 .Lmid_exit_l2
	s_setprio 3
	ds_bpermute_b32 v6, v55, v96
	ds_bpermute_b32 v7, v85, v96
	ds_bpermute_b32 v8, v86, v96
	ds_bpermute_b32 v9, v87, v96
	s_waitcnt lgkmcnt(3)
	v_and_b32_e32 v46, 0xffff, v6
	s_waitcnt lgkmcnt(2)
	v_and_b32_e32 v50, 0xffff, v7
	v_lshlrev_b32_e32 v42, 7, v46
	v_lshl_add_u64 v[6:7], v[44:45], 0, v[42:43]
	v_lshlrev_b32_e32 v42, 7, v50
	s_waitcnt lgkmcnt(1)
	v_and_b32_e32 v53, 0xffff, v8
	global_load_dwordx4 v[30:33], v[6:7], off
	v_lshl_add_u64 v[6:7], v[44:45], 0, v[42:43]
	v_lshlrev_b32_e32 v42, 7, v53
	s_waitcnt lgkmcnt(0)
	v_and_b32_e32 v59, 0xffff, v9
	global_load_dwordx4 v[18:21], v[6:7], off
	v_lshl_add_u64 v[6:7], v[44:45], 0, v[42:43]
	v_lshlrev_b32_e32 v42, 7, v59
	global_load_dwordx4 v[10:13], v[6:7], off
	v_lshl_add_u64 v[6:7], v[44:45], 0, v[42:43]
	global_load_dwordx4 v[6:9], v[6:7], off
	v_mul_hi_u32 v42, v46, s19
	v_lshlrev_b32_e32 v42, 2, v42
	ds_read_b32 v56, v42 offset:34816
	v_mul_hi_u32 v42, v50, s19
	v_lshlrev_b32_e32 v42, 2, v42
	ds_read_b32 v57, v42 offset:34816
	v_mul_hi_u32 v42, v53, s19
	v_lshlrev_b32_e32 v42, 2, v42
	ds_read_b32 v50, v42 offset:34816
	v_mul_hi_u32 v42, v59, s19
	v_lshlrev_b32_e32 v42, 2, v42
	ds_read_b32 v46, v42 offset:34816
	s_setprio 1
	v_and_b32_e32 v42, 16, v52
	v_cmp_ne_u32_e64 s[0:1], 0, v42
	s_and_saveexec_b64 s[4:5], s[0:1]
	s_cbranch_execz .LBB3_17
	v_and_b32_e32 v42, 63, v98
	v_mul_u32_u24_e32 v42, 0x220, v42
	v_or_b32_e32 v42, v49, v42
	ds_read2_b32 v[98:99], v42 offset1:8
	ds_read2_b32 v[100:101], v42 offset0:16 offset1:24
	ds_read2_b32 v[102:103], v42 offset0:32 offset1:40
	s_waitcnt lgkmcnt(2)
	v_add_f32_e32 v53, v78, v98
	v_add_f32_e32 v59, v79, v99
	s_waitcnt lgkmcnt(1)
	v_add_f32_e32 v63, v76, v100
	ds_write2_b32 v42, v53, v59 offset1:8
	v_add_f32_e32 v53, v77, v101
	ds_read2_b32 v[76:77], v42 offset0:48 offset1:56
	ds_write2_b32 v42, v63, v53 offset0:16 offset1:24
	s_waitcnt lgkmcnt(3)
	v_add_f32_e32 v53, v74, v102
	v_add_f32_e32 v59, v75, v103
	ds_read2_b32 v[74:75], v42 offset0:64 offset1:72
	ds_write2_b32 v42, v53, v59 offset0:32 offset1:40
	s_waitcnt lgkmcnt(3)
	v_add_f32_e32 v53, v72, v76
	v_add_f32_e32 v59, v73, v77
	ds_read2_b32 v[72:73], v42 offset0:80 offset1:88
	ds_write2_b32 v42, v53, v59 offset0:48 offset1:56
	s_waitcnt lgkmcnt(3)
	v_add_f32_e32 v53, v70, v74
	v_add_f32_e32 v59, v71, v75
	ds_read2_b32 v[70:71], v42 offset0:96 offset1:104
	ds_write2_b32 v42, v53, v59 offset0:64 offset1:72
	s_waitcnt lgkmcnt(3)
	v_add_f32_e32 v53, v68, v72
	v_add_f32_e32 v59, v69, v73
	ds_read2_b32 v[68:69], v42 offset0:112 offset1:120
	ds_bpermute_b32 v63, v90, v95
	ds_write2_b32 v42, v53, v59 offset0:80 offset1:88
	s_waitcnt lgkmcnt(4)
	v_add_f32_e32 v53, v66, v70
	v_add_f32_e32 v59, v67, v71
	ds_write2_b32 v42, v53, v59 offset0:96 offset1:104
	s_waitcnt lgkmcnt(3)
	v_add_f32_e32 v53, v64, v68
	v_mov_b32_e32 v64, 0
	v_add_f32_e32 v59, v65, v69
	s_waitcnt lgkmcnt(2)
	v_lshrrev_b32_e32 v98, 16, v63
	v_mov_b32_e32 v65, v64
	v_mov_b32_e32 v78, v64
	v_mov_b32_e32 v79, v64
	v_mov_b32_e32 v76, v64
	v_mov_b32_e32 v77, v64
	v_mov_b32_e32 v74, v64
	v_mov_b32_e32 v75, v64
	v_mov_b32_e32 v72, v64
	v_mov_b32_e32 v73, v64
	v_mov_b32_e32 v70, v64
	v_mov_b32_e32 v71, v64
	v_mov_b32_e32 v68, v64
	v_mov_b32_e32 v69, v64
	v_mov_b32_e32 v66, v64
	v_mov_b32_e32 v67, v64
	ds_write2_b32 v42, v53, v59 offset0:112 offset1:120
